# baseline (speedup 1.0000x reference)
.Lg_top:
	s_mov_b32 s43, 0
	s_cmp_ge_u32 s10, s9
	s_cbranch_scc1 .Lg_drain0
	s_cmp_eq_u32 s10, 6
	s_cselect_b32 s12, s45, s12
	v_readlane_b32 s13, v247, s10
	s_add_u32 s14, s12, 0x4b0
	s_add_u32 s15, s12, 0x960
	s_add_u32 s16, s12, 0xe10
	s_nop 1
	s_and_b32 s18, s13, 0xff
	s_cmp_eq_u32 s18, 1
	s_cselect_b32 s42, s12, 0x80000000
	s_and_b32 s18, s13, 0xff00
	s_cmp_eq_u32 s18, 0x100
	s_cselect_b32 s14, s14, 0x80000000
	s_and_b32 s18, s13, 0xff0000
	s_cmp_eq_u32 s18, 0x10000
	s_cselect_b32 s15, s15, 0x80000000
	s_and_b32 s18, s13, 0xff000000
	s_cmp_eq_u32 s18, 0x1000000
	s_cselect_b32 s16, s16, 0x80000000
	v_lshrrev_b32_e64 v249, v240, s13
	v_and_b32_e32 v249, 0xff, v249
	v_cmp_eq_u32_e32 vcc, 1, v249
	s_nop 1
	v_cndmask_b32_e32 v254, v255, v239, vcc
	s_sub_u32 s18, s10, 2
	s_cmp_lt_u32 s18, s9
	s_cbranch_scc0 .Lg_s2skip0
	s_waitcnt vmcnt(21)
	v_cvt_pk_f16_f32 v250, v138, v139
	v_cvt_pk_f16_f32 v251, v140, v141
	ds_write_b64 v241, v[250:251] offset:0
	buffer_load_dwordx4 v[138:141], v238, s[20:23], s42 offen nt
	s_waitcnt vmcnt(21)
	v_cvt_pk_f16_f32 v252, v142, v143
	v_cvt_pk_f16_f32 v253, v144, v145
	ds_write_b64 v241, v[252:253] offset:600
	buffer_load_dwordx4 v[142:145], v238, s[24:27], s42 offen nt
	s_waitcnt vmcnt(21)
	v_cvt_pk_f16_f32 v250, v146, v147
	v_cvt_pk_f16_f32 v251, v148, v149
	ds_write_b64 v241, v[250:251] offset:1248
	buffer_load_dwordx4 v[146:149], v238, s[20:23], s14 offen nt
	s_waitcnt vmcnt(21)
	v_cvt_pk_f16_f32 v252, v150, v151
	v_cvt_pk_f16_f32 v253, v152, v153
	ds_write_b64 v241, v[252:253] offset:1848
	buffer_load_dwordx4 v[150:153], v238, s[24:27], s14 offen nt
	s_waitcnt vmcnt(21)
	v_cvt_pk_f16_f32 v250, v154, v155
	v_cvt_pk_f16_f32 v251, v156, v157
	ds_write_b64 v241, v[250:251] offset:2496
	buffer_load_dwordx4 v[154:157], v238, s[20:23], s15 offen nt
	s_waitcnt vmcnt(21)
	v_cvt_pk_f16_f32 v252, v158, v159
	v_cvt_pk_f16_f32 v253, v160, v161
	ds_write_b64 v241, v[252:253] offset:3096
	buffer_load_dwordx4 v[158:161], v238, s[24:27], s15 offen nt
	s_waitcnt vmcnt(21)
	v_cvt_pk_f16_f32 v250, v162, v163
	v_cvt_pk_f16_f32 v251, v164, v165
	ds_write_b64 v241, v[250:251] offset:3744
	buffer_load_dwordx4 v[162:165], v238, s[20:23], s16 offen nt
	s_waitcnt vmcnt(21)
	v_cvt_pk_f16_f32 v252, v166, v167
	v_cvt_pk_f16_f32 v253, v168, v169
	ds_write_b64 v241, v[252:253] offset:4344
	buffer_load_dwordx4 v[166:169], v238, s[24:27], s16 offen nt
	s_mov_b64 exec, s[34:35]
	s_waitcnt vmcnt(21)
	v_cvt_pk_f16_f32 v250, v170, v171
	v_cvt_pk_f16_f32 v251, v172, v173
	ds_write_b64 v242, v[250:251] offset:0
	s_mov_b64 exec, -1
	buffer_load_dwordx4 v[170:173], v254, s[20:23], s12 offen nt
	s_mov_b64 exec, s[34:35]
	s_waitcnt vmcnt(21)
	v_cvt_pk_f16_f32 v252, v174, v175
	v_cvt_pk_f16_f32 v253, v176, v177
	ds_write_b64 v242, v[252:253] offset:600
	s_mov_b64 exec, -1
	buffer_load_dwordx4 v[174:177], v254, s[24:27], s12 offen nt
	s_branch .Lg_s1done0
.Lg_s2skip0:
	buffer_load_dwordx4 v[138:141], v238, s[20:23], s42 offen nt
	buffer_load_dwordx4 v[142:145], v238, s[24:27], s42 offen nt
	buffer_load_dwordx4 v[146:149], v238, s[20:23], s14 offen nt
	buffer_load_dwordx4 v[150:153], v238, s[24:27], s14 offen nt
	buffer_load_dwordx4 v[154:157], v238, s[20:23], s15 offen nt
	buffer_load_dwordx4 v[158:161], v238, s[24:27], s15 offen nt
	buffer_load_dwordx4 v[162:165], v238, s[20:23], s16 offen nt
	buffer_load_dwordx4 v[166:169], v238, s[24:27], s16 offen nt
	buffer_load_dwordx4 v[170:173], v254, s[20:23], s12 offen nt
	buffer_load_dwordx4 v[174:177], v254, s[24:27], s12 offen nt
	s_branch .Lg_s1done0
.Lg_drain0:
	s_mov_b32 s43, 1

.Lg_s3skip0:
	s_cmp_eq_u32 s10, 10
	s_cselect_b32 s32, s46, s32
	s_sub_u32 s18, s10, 4
	s_cmp_lt_u32 s18, s9
	s_cselect_b32 s19, s32, 0x80000000
	ds_read_b128 v[226:229], v245 offset:0
	s_add_u32 s32, s32, 0x40000
	s_waitcnt lgkmcnt(0)
	buffer_store_dwordx4 v[226:229], v246, s[28:31], s19 offen nt
	s_cmp_eq_u32 s43, 0
	s_cbranch_scc1 .Lg_tail0
	s_sub_u32 s18, s10, 2
	s_cmp_lt_u32 s18, s9
	s_cbranch_scc0 .Lg_tail0
	s_cmp_gt_u32 s10, s9
	s_cbranch_scc1 .Lg_s2finalb0
	s_waitcnt vmcnt(22)
	v_cvt_pk_f16_f32 v250, v138, v139
	v_cvt_pk_f16_f32 v251, v140, v141
	ds_write_b64 v241, v[250:251] offset:0
	s_waitcnt vmcnt(21)
	v_cvt_pk_f16_f32 v252, v142, v143
	v_cvt_pk_f16_f32 v253, v144, v145
	ds_write_b64 v241, v[252:253] offset:600
	s_waitcnt vmcnt(20)
	v_cvt_pk_f16_f32 v250, v146, v147
	v_cvt_pk_f16_f32 v251, v148, v149
	ds_write_b64 v241, v[250:251] offset:1248
	s_waitcnt vmcnt(19)
	v_cvt_pk_f16_f32 v252, v150, v151
	v_cvt_pk_f16_f32 v253, v152, v153
	ds_write_b64 v241, v[252:253] offset:1848
	s_waitcnt vmcnt(18)
	v_cvt_pk_f16_f32 v250, v154, v155
	v_cvt_pk_f16_f32 v251, v156, v157
	ds_write_b64 v241, v[250:251] offset:2496
	s_waitcnt vmcnt(17)
	v_cvt_pk_f16_f32 v252, v158, v159
	v_cvt_pk_f16_f32 v253, v160, v161
	ds_write_b64 v241, v[252:253] offset:3096
	s_waitcnt vmcnt(16)
	v_cvt_pk_f16_f32 v250, v162, v163
	v_cvt_pk_f16_f32 v251, v164, v165
	ds_write_b64 v241, v[250:251] offset:3744
	s_waitcnt vmcnt(15)
	v_cvt_pk_f16_f32 v252, v166, v167
	v_cvt_pk_f16_f32 v253, v168, v169
	ds_write_b64 v241, v[252:253] offset:4344
	s_mov_b64 exec, s[34:35]
	s_waitcnt vmcnt(14)
	v_cvt_pk_f16_f32 v250, v170, v171
	v_cvt_pk_f16_f32 v251, v172, v173
	ds_write_b64 v242, v[250:251] offset:0
	s_mov_b64 exec, -1
	s_mov_b64 exec, s[34:35]
	s_waitcnt vmcnt(13)
	v_cvt_pk_f16_f32 v252, v174, v175
	v_cvt_pk_f16_f32 v253, v176, v177
	ds_write_b64 v242, v[252:253] offset:600
	s_mov_b64 exec, -1
	s_branch .Lg_s2fdone0
.Lg_s2finalb0:
	s_waitcnt vmcnt(12)
	v_cvt_pk_f16_f32 v250, v138, v139
	v_cvt_pk_f16_f32 v251, v140, v141
	ds_write_b64 v241, v[250:251] offset:0
	s_waitcnt vmcnt(11)
	v_cvt_pk_f16_f32 v252, v142, v143
	v_cvt_pk_f16_f32 v253, v144, v145
	ds_write_b64 v241, v[252:253] offset:600
	s_waitcnt vmcnt(10)
	v_cvt_pk_f16_f32 v250, v146, v147
	v_cvt_pk_f16_f32 v251, v148, v149
	ds_write_b64 v241, v[250:251] offset:1248
	s_waitcnt vmcnt(9)
	v_cvt_pk_f16_f32 v252, v150, v151
	v_cvt_pk_f16_f32 v253, v152, v153
	ds_write_b64 v241, v[252:253] offset:1848
	s_waitcnt vmcnt(8)
	v_cvt_pk_f16_f32 v250, v154, v155
	v_cvt_pk_f16_f32 v251, v156, v157
	ds_write_b64 v241, v[250:251] offset:2496
	s_waitcnt vmcnt(7)
	v_cvt_pk_f16_f32 v252, v158, v159
	v_cvt_pk_f16_f32 v253, v160, v161
	ds_write_b64 v241, v[252:253] offset:3096
	s_waitcnt vmcnt(6)
	v_cvt_pk_f16_f32 v250, v162, v163
	v_cvt_pk_f16_f32 v251, v164, v165
	ds_write_b64 v241, v[250:251] offset:3744
	s_waitcnt vmcnt(5)
	v_cvt_pk_f16_f32 v252, v166, v167
	v_cvt_pk_f16_f32 v253, v168, v169
	ds_write_b64 v241, v[252:253] offset:4344
	s_mov_b64 exec, s[34:35]
	s_waitcnt vmcnt(4)
	v_cvt_pk_f16_f32 v250, v170, v171
	v_cvt_pk_f16_f32 v251, v172, v173
	ds_write_b64 v242, v[250:251] offset:0
	s_mov_b64 exec, -1
	s_mov_b64 exec, s[34:35]
	s_waitcnt vmcnt(3)
	v_cvt_pk_f16_f32 v252, v174, v175
	v_cvt_pk_f16_f32 v253, v176, v177
	ds_write_b64 v242, v[252:253] offset:600
	s_mov_b64 exec, -1
.Lg_s2fdone0:
	s_waitcnt lgkmcnt(0)
.Lg_tail0:
	s_barrier
	s_add_u32 s10, s10, 1
	s_cmp_ge_u32 s10, s11
	s_cbranch_scc1 .Lg_end
.Lg_half1:
	s_mov_b32 s43, 0
	s_cmp_ge_u32 s10, s9
	s_cbranch_scc1 .Lg_drain1
	s_cmp_eq_u32 s10, 6
	s_cselect_b32 s12, s45, s12
	v_readlane_b32 s13, v247, s10
	s_add_u32 s14, s12, 0x4b0
	s_add_u32 s15, s12, 0x960
	s_add_u32 s16, s12, 0xe10
	s_nop 1
	s_and_b32 s18, s13, 0xff
	s_cmp_eq_u32 s18, 1
	s_cselect_b32 s42, s12, 0x80000000
	s_and_b32 s18, s13, 0xff00
	s_cmp_eq_u32 s18, 0x100
	s_cselect_b32 s14, s14, 0x80000000
	s_and_b32 s18, s13, 0xff0000
	s_cmp_eq_u32 s18, 0x10000
	s_cselect_b32 s15, s15, 0x80000000
	s_and_b32 s18, s13, 0xff000000
	s_cmp_eq_u32 s18, 0x1000000
	s_cselect_b32 s16, s16, 0x80000000
	v_lshrrev_b32_e64 v249, v240, s13
	v_and_b32_e32 v249, 0xff, v249
	v_cmp_eq_u32_e32 vcc, 1, v249
	s_nop 1
	v_cndmask_b32_e32 v254, v255, v239, vcc
	s_sub_u32 s18, s10, 2
	s_cmp_lt_u32 s18, s9
	s_cbranch_scc0 .Lg_s2skip1
	s_waitcnt vmcnt(21)
	v_cvt_pk_f16_f32 v250, v178, v179
	v_cvt_pk_f16_f32 v251, v180, v181
	ds_write_b64 v241, v[250:251] offset:19968
	buffer_load_dwordx4 v[178:181], v238, s[20:23], s42 offen nt
	s_waitcnt vmcnt(21)
	v_cvt_pk_f16_f32 v252, v182, v183
	v_cvt_pk_f16_f32 v253, v184, v185
	ds_write_b64 v241, v[252:253] offset:20568
	buffer_load_dwordx4 v[182:185], v238, s[24:27], s42 offen nt
	s_waitcnt vmcnt(21)
	v_cvt_pk_f16_f32 v250, v186, v187
	v_cvt_pk_f16_f32 v251, v188, v189
	ds_write_b64 v241, v[250:251] offset:21216
	buffer_load_dwordx4 v[186:189], v238, s[20:23], s14 offen nt
	s_waitcnt vmcnt(21)
	v_cvt_pk_f16_f32 v252, v190, v191
	v_cvt_pk_f16_f32 v253, v192, v193
	ds_write_b64 v241, v[252:253] offset:21816
	buffer_load_dwordx4 v[190:193], v238, s[24:27], s14 offen nt
	s_waitcnt vmcnt(21)
	v_cvt_pk_f16_f32 v250, v194, v195
	v_cvt_pk_f16_f32 v251, v196, v197
	ds_write_b64 v241, v[250:251] offset:22464
	buffer_load_dwordx4 v[194:197], v238, s[20:23], s15 offen nt
	s_waitcnt vmcnt(21)
	v_cvt_pk_f16_f32 v252, v198, v199
	v_cvt_pk_f16_f32 v253, v200, v201
	ds_write_b64 v241, v[252:253] offset:23064
	buffer_load_dwordx4 v[198:201], v238, s[24:27], s15 offen nt
	s_waitcnt vmcnt(21)
	v_cvt_pk_f16_f32 v250, v202, v203
	v_cvt_pk_f16_f32 v251, v204, v205
	ds_write_b64 v241, v[250:251] offset:23712
	buffer_load_dwordx4 v[202:205], v238, s[20:23], s16 offen nt
	s_waitcnt vmcnt(21)
	v_cvt_pk_f16_f32 v252, v206, v207
	v_cvt_pk_f16_f32 v253, v208, v209
	ds_write_b64 v241, v[252:253] offset:24312
	buffer_load_dwordx4 v[206:209], v238, s[24:27], s16 offen nt
	s_mov_b64 exec, s[34:35]
	s_waitcnt vmcnt(21)
	v_cvt_pk_f16_f32 v250, v210, v211
	v_cvt_pk_f16_f32 v251, v212, v213
	ds_write_b64 v242, v[250:251] offset:19968
	s_mov_b64 exec, -1
	buffer_load_dwordx4 v[210:213], v254, s[20:23], s12 offen nt
	s_mov_b64 exec, s[34:35]
	s_waitcnt vmcnt(21)
	v_cvt_pk_f16_f32 v252, v214, v215
	v_cvt_pk_f16_f32 v253, v216, v217
	ds_write_b64 v242, v[252:253] offset:20568
	s_mov_b64 exec, -1
	buffer_load_dwordx4 v[214:217], v254, s[24:27], s12 offen nt
	s_branch .Lg_s1done1
.Lg_s2skip1:
	buffer_load_dwordx4 v[178:181], v238, s[20:23], s42 offen nt
	buffer_load_dwordx4 v[182:185], v238, s[24:27], s42 offen nt
	buffer_load_dwordx4 v[186:189], v238, s[20:23], s14 offen nt
	buffer_load_dwordx4 v[190:193], v238, s[24:27], s14 offen nt
	buffer_load_dwordx4 v[194:197], v238, s[20:23], s15 offen nt
	buffer_load_dwordx4 v[198:201], v238, s[24:27], s15 offen nt
	buffer_load_dwordx4 v[202:205], v238, s[20:23], s16 offen nt
	buffer_load_dwordx4 v[206:209], v238, s[24:27], s16 offen nt
	buffer_load_dwordx4 v[210:213], v254, s[20:23], s12 offen nt
	buffer_load_dwordx4 v[214:217], v254, s[24:27], s12 offen nt
	s_branch .Lg_s1done1

.Lg_s3skip1:
	s_cmp_eq_u32 s10, 10
	s_cselect_b32 s32, s46, s32
	s_sub_u32 s18, s10, 4
	s_cmp_lt_u32 s18, s9
	s_cselect_b32 s19, s32, 0x80000000
	ds_read_b128 v[226:229], v245 offset:4352
	s_add_u32 s32, s32, 0x40000
	s_waitcnt lgkmcnt(0)
	buffer_store_dwordx4 v[226:229], v246, s[28:31], s19 offen nt
	s_cmp_eq_u32 s43, 0
	s_cbranch_scc1 .Lg_tail1
	s_sub_u32 s18, s10, 2
	s_cmp_lt_u32 s18, s9
	s_cbranch_scc0 .Lg_tail1
	s_cmp_gt_u32 s10, s9
	s_cbranch_scc1 .Lg_s2finalb1
	s_waitcnt vmcnt(22)
	v_cvt_pk_f16_f32 v250, v178, v179
	v_cvt_pk_f16_f32 v251, v180, v181
	ds_write_b64 v241, v[250:251] offset:19968
	s_waitcnt vmcnt(21)
	v_cvt_pk_f16_f32 v252, v182, v183
	v_cvt_pk_f16_f32 v253, v184, v185
	ds_write_b64 v241, v[252:253] offset:20568
	s_waitcnt vmcnt(20)
	v_cvt_pk_f16_f32 v250, v186, v187
	v_cvt_pk_f16_f32 v251, v188, v189
	ds_write_b64 v241, v[250:251] offset:21216
	s_waitcnt vmcnt(19)
	v_cvt_pk_f16_f32 v252, v190, v191
	v_cvt_pk_f16_f32 v253, v192, v193
	ds_write_b64 v241, v[252:253] offset:21816
	s_waitcnt vmcnt(18)
	v_cvt_pk_f16_f32 v250, v194, v195
	v_cvt_pk_f16_f32 v251, v196, v197
	ds_write_b64 v241, v[250:251] offset:22464
	s_waitcnt vmcnt(17)
	v_cvt_pk_f16_f32 v252, v198, v199
	v_cvt_pk_f16_f32 v253, v200, v201
	ds_write_b64 v241, v[252:253] offset:23064
	s_waitcnt vmcnt(16)
	v_cvt_pk_f16_f32 v250, v202, v203
	v_cvt_pk_f16_f32 v251, v204, v205
	ds_write_b64 v241, v[250:251] offset:23712
	s_waitcnt vmcnt(15)
	v_cvt_pk_f16_f32 v252, v206, v207
	v_cvt_pk_f16_f32 v253, v208, v209
	ds_write_b64 v241, v[252:253] offset:24312
	s_mov_b64 exec, s[34:35]
	s_waitcnt vmcnt(14)
	v_cvt_pk_f16_f32 v250, v210, v211
	v_cvt_pk_f16_f32 v251, v212, v213
	ds_write_b64 v242, v[250:251] offset:19968
	s_mov_b64 exec, -1
	s_mov_b64 exec, s[34:35]
	s_waitcnt vmcnt(13)
	v_cvt_pk_f16_f32 v252, v214, v215
	v_cvt_pk_f16_f32 v253, v216, v217
	ds_write_b64 v242, v[252:253] offset:20568
	s_mov_b64 exec, -1
	s_branch .Lg_s2fdone1
.Lg_s2finalb1:
	s_waitcnt vmcnt(12)
	v_cvt_pk_f16_f32 v250, v178, v179
	v_cvt_pk_f16_f32 v251, v180, v181
	ds_write_b64 v241, v[250:251] offset:19968
	s_waitcnt vmcnt(11)
	v_cvt_pk_f16_f32 v252, v182, v183
	v_cvt_pk_f16_f32 v253, v184, v185
	ds_write_b64 v241, v[252:253] offset:20568
	s_waitcnt vmcnt(10)
	v_cvt_pk_f16_f32 v250, v186, v187
	v_cvt_pk_f16_f32 v251, v188, v189
	ds_write_b64 v241, v[250:251] offset:21216
	s_waitcnt vmcnt(9)
	v_cvt_pk_f16_f32 v252, v190, v191
	v_cvt_pk_f16_f32 v253, v192, v193
	ds_write_b64 v241, v[252:253] offset:21816
	s_waitcnt vmcnt(8)
	v_cvt_pk_f16_f32 v250, v194, v195
	v_cvt_pk_f16_f32 v251, v196, v197
	ds_write_b64 v241, v[250:251] offset:22464
	s_waitcnt vmcnt(7)
	v_cvt_pk_f16_f32 v252, v198, v199
	v_cvt_pk_f16_f32 v253, v200, v201
	ds_write_b64 v241, v[252:253] offset:23064
	s_waitcnt vmcnt(6)
	v_cvt_pk_f16_f32 v250, v202, v203
	v_cvt_pk_f16_f32 v251, v204, v205
	ds_write_b64 v241, v[250:251] offset:23712
	s_waitcnt vmcnt(5)
	v_cvt_pk_f16_f32 v252, v206, v207
	v_cvt_pk_f16_f32 v253, v208, v209
	ds_write_b64 v241, v[252:253] offset:24312
	s_mov_b64 exec, s[34:35]
	s_waitcnt vmcnt(4)
	v_cvt_pk_f16_f32 v250, v210, v211
	v_cvt_pk_f16_f32 v251, v212, v213
	ds_write_b64 v242, v[250:251] offset:19968
	s_mov_b64 exec, -1
	s_mov_b64 exec, s[34:35]
	s_waitcnt vmcnt(3)
	v_cvt_pk_f16_f32 v252, v214, v215
	v_cvt_pk_f16_f32 v253, v216, v217
	ds_write_b64 v242, v[252:253] offset:20568
	s_mov_b64 exec, -1

.Lg_tail1:
	s_barrier
	s_add_u32 s10, s10, 1
	s_cmp_lt_u32 s10, s11
	s_cbranch_scc1 .Lg_top
